# P4b merge epilogue: running sum of row group 5 also kept on chip, in 16 KB static LDS above the dynamic 144 KB (group_segment_fixed_size 16384)
# speedup vs baseline: 1.0399x; 1.0045x over previous
.LBB0_822:
	v_add_f32_e32 v110, v110, v14
	v_add_f32_e32 v111, v111, v15
	v_mul_f32_e32 v110, 0xbfb8aa3b, v110
	v_mul_f32_e32 v111, 0xbfb8aa3b, v111
	v_exp_f32_e32 v110, v110
	v_exp_f32_e32 v111, v111
	s_waitcnt vmcnt(5)
	v_lshlrev_b32_e32 v126, 16, v26
	v_and_b32_e32 v127, 0xffff0000, v26
	v_add_f32_e32 v26, v112, v16
	v_mul_f32_e32 v26, 0xbfb8aa3b, v26
	v_add_f32_e32 v112, v113, v17
	v_exp_f32_e32 v26, v26
	v_mul_f32_e32 v112, 0xbfb8aa3b, v112
	v_exp_f32_e32 v113, v112
	v_add_f32_e32 v110, 1.0, v110
	v_add_f32_e32 v111, 1.0, v111
	v_rcp_f32_e32 v110, v110
	v_rcp_f32_e32 v111, v111
	v_add_f32_e32 v106, v106, v10
	v_add_f32_e32 v26, 1.0, v26
	v_mul_f32_e32 v106, 0xbfb8aa3b, v106
	v_rcp_f32_e32 v112, v26
	v_add_f32_e32 v26, 1.0, v113
	v_exp_f32_e32 v115, v106
	v_add_f32_e32 v106, v107, v11
	v_lshlrev_b32_e32 v128, 16, v138
	v_and_b32_e32 v129, 0xffff0000, v138
	v_rcp_f32_e32 v113, v26
	v_mul_f32_e32 v106, 0xbfb8aa3b, v106
	v_pk_fma_f32 v[110:111], v[110:111], v[126:127], v[128:129]
	v_exp_f32_e32 v128, v106
	v_lshlrev_b32_e32 v26, 16, v27
	v_and_b32_e32 v27, 0xffff0000, v27
	v_lshlrev_b32_e32 v126, 16, v139
	v_and_b32_e32 v127, 0xffff0000, v139
	v_pk_fma_f32 v[106:107], v[112:113], v[26:27], v[126:127]
	v_lshlrev_b32_e32 v112, 16, v28
	v_and_b32_e32 v113, 0xffff0000, v28
	v_add_f32_e32 v28, v108, v12
	v_add_f32_e32 v108, v109, v13
	v_add_f32_e32 v26, 1.0, v115
	v_add_f32_e32 v27, 1.0, v128
	v_mul_f32_e32 v28, 0xbfb8aa3b, v28
	v_mul_f32_e32 v108, 0xbfb8aa3b, v108
	v_rcp_f32_e32 v26, v26
	v_rcp_f32_e32 v27, v27
	v_exp_f32_e32 v28, v28
	v_exp_f32_e32 v115, v108
	v_lshlrev_b32_e32 v126, 16, v136
	v_and_b32_e32 v127, 0xffff0000, v136
	v_pk_fma_f32 v[108:109], v[26:27], v[112:113], v[126:127]
	v_add_f32_e32 v26, 1.0, v28
	v_add_f32_e32 v27, 1.0, v115
	v_rcp_f32_e32 v26, v26
	v_rcp_f32_e32 v27, v27
	v_add_f32_e32 v102, v102, v6
	v_add_f32_e32 v103, v103, v7
	v_lshlrev_b32_e32 v28, 16, v29
	v_and_b32_e32 v29, 0xffff0000, v29
	v_lshlrev_b32_e32 v112, 16, v137
	v_and_b32_e32 v113, 0xffff0000, v137
	v_mul_f32_e32 v102, 0xbfb8aa3b, v102
	v_mul_f32_e32 v103, 0xbfb8aa3b, v103
	v_pk_fma_f32 v[112:113], v[26:27], v[28:29], v[112:113]
	v_exp_f32_e32 v102, v102
	v_exp_f32_e32 v103, v103
	v_cvt_pk_bf16_f32 v26, v110, v111
	v_cvt_pk_bf16_f32 v27, v106, v107
	v_cvt_pk_bf16_f32 v28, v108, v109
	v_cvt_pk_bf16_f32 v29, v112, v113
	v_lshl_add_u64 v[106:107], v[134:135], 0, v[0:1]
	v_mov_b32_e32 v218, v26
	v_mov_b32_e32 v219, v27
	v_mov_b32_e32 v242, v28
	v_mov_b32_e32 v243, v29
	s_mov_b64 exec, s[34:35]
	global_store_dwordx4 v[106:107], v[26:29], off
	s_mov_b64 exec, -1
	v_add_f32_e32 v98, v98, v2
	v_add_f32_e32 v99, v99, v3
	s_waitcnt vmcnt(5)
	v_lshlrev_b32_e32 v28, 16, v18
	v_and_b32_e32 v29, 0xffff0000, v18
	v_add_f32_e32 v18, v104, v8
	v_mul_f32_e32 v18, 0xbfb8aa3b, v18
	v_add_f32_e32 v104, v105, v9
	v_add_f32_e32 v26, 1.0, v102
	v_add_f32_e32 v27, 1.0, v103
	v_exp_f32_e32 v18, v18
	v_mul_f32_e32 v104, 0xbfb8aa3b, v104
	v_rcp_f32_e32 v26, v26
	v_rcp_f32_e32 v27, v27
	v_exp_f32_e32 v104, v104
	v_lshlrev_b32_e32 v102, 16, v132
	v_and_b32_e32 v103, 0xffff0000, v132
	v_add_f32_e32 v18, 1.0, v18
	v_pk_fma_f32 v[26:27], v[26:27], v[28:29], v[102:103]
	v_rcp_f32_e32 v28, v18
	v_add_f32_e32 v18, 1.0, v104
	v_mul_f32_e32 v98, 0xbfb8aa3b, v98
	v_mul_f32_e32 v99, 0xbfb8aa3b, v99
	v_rcp_f32_e32 v29, v18
	v_exp_f32_e32 v98, v98
	v_exp_f32_e32 v99, v99
	v_lshlrev_b32_e32 v18, 16, v19
	v_and_b32_e32 v19, 0xffff0000, v19
	v_lshlrev_b32_e32 v102, 16, v133
	v_and_b32_e32 v103, 0xffff0000, v133
	v_pk_fma_f32 v[28:29], v[28:29], v[18:19], v[102:103]
	v_add_f32_e32 v18, 1.0, v98
	v_add_f32_e32 v19, 1.0, v99
	v_lshlrev_b32_e32 v98, 16, v20
	v_and_b32_e32 v99, 0xffff0000, v20
	v_add_f32_e32 v20, v100, v4
	v_add_f32_e32 v100, v101, v5
	v_mul_f32_e32 v20, 0xbfb8aa3b, v20
	v_mul_f32_e32 v100, 0xbfb8aa3b, v100
	v_rcp_f32_e32 v18, v18
	v_rcp_f32_e32 v19, v19
	v_exp_f32_e32 v20, v20
	v_exp_f32_e32 v100, v100
	v_lshlrev_b32_e32 v102, 16, v130
	v_and_b32_e32 v103, 0xffff0000, v130
	v_pk_fma_f32 v[98:99], v[18:19], v[98:99], v[102:103]
	v_add_f32_e32 v18, 1.0, v20
	v_add_f32_e32 v19, 1.0, v100
	v_rcp_f32_e32 v18, v18
	v_rcp_f32_e32 v19, v19
	v_lshlrev_b32_e32 v20, 16, v21
	v_and_b32_e32 v21, 0xffff0000, v21
	v_lshlrev_b32_e32 v100, 16, v131
	v_and_b32_e32 v101, 0xffff0000, v131
	v_pk_fma_f32 v[100:101], v[18:19], v[20:21], v[100:101]
	v_cvt_pk_bf16_f32 v18, v26, v27
	v_cvt_pk_bf16_f32 v19, v28, v29
	v_cvt_pk_bf16_f32 v20, v98, v99
	v_cvt_pk_bf16_f32 v21, v100, v101
	v_mov_b32_e32 v244, v18
	v_mov_b32_e32 v245, v19
	v_mov_b32_e32 v211, v20
	v_mov_b32_e32 v212, v21
	s_mov_b64 exec, s[34:35]
	global_store_dwordx4 v[106:107], v[18:21], off offset:256
	s_mov_b64 exec, -1
	v_mov_b32_e32 v100, 0
	s_and_b64 vcc, exec, s[0:1]
	v_or_b32_e32 v20, 16, v114
	v_mov_b64_e32 v[18:19], s[12:13]
	v_mad_i64_i32 v[18:19], s[28:29], v20, s66, v[18:19]
	v_lshl_add_u64 v[18:19], s[26:27], 1, v[18:19]
	v_lshl_add_u64 v[18:19], v[18:19], 0, v[0:1]
	global_load_dwordx4 v[26:29], v[18:19], off
	v_ashrrev_i32_e32 v21, 31, v20
	v_lshlrev_b64 v[20:21], 11, v[20:21]
	v_lshl_add_u64 v[102:103], s[10:11], 0, v[20:21]
	v_mov_b32_e32 v106, 0
	v_mov_b32_e32 v107, 0
	v_mov_b32_e32 v104, 0
	v_mov_b32_e32 v105, 0
	s_cbranch_vccnz .LBB0_824
	v_lshl_add_u64 v[20:21], v[102:103], 0, v[0:1]
	ds_read_b64 v[106:107], v222 offset:16192
	s_waitcnt lgkmcnt(0)
	ds_read_b64 v[104:105], v222 offset:16200
	s_waitcnt lgkmcnt(0)
.LBB0_824:
	s_nop 0
	global_load_dwordx4 v[18:21], v[18:19], off offset:256
	s_and_b64 vcc, exec, s[0:1]
	v_mov_b32_e32 v101, 0
	v_mov_b32_e32 v98, 0
	v_mov_b32_e32 v99, 0
	s_cbranch_vccnz .LBB0_826
	v_lshl_add_u64 v[98:99], v[102:103], 0, v[0:1]
	ds_read_b64 v[100:101], v222 offset:24384
	s_waitcnt lgkmcnt(0)
	s_nop 0
	ds_read_b64 v[98:99], v222 offset:24392
	s_waitcnt lgkmcnt(0)

.LBB0_830:
	v_add_f32_e32 v78, v78, v14
	v_add_f32_e32 v79, v79, v15
	v_mul_f32_e32 v78, 0xbfb8aa3b, v78
	v_mul_f32_e32 v79, 0xbfb8aa3b, v79
	v_exp_f32_e32 v78, v78
	v_exp_f32_e32 v79, v79
	s_waitcnt vmcnt(5)
	v_lshlrev_b32_e32 v92, 16, v26
	v_and_b32_e32 v93, 0xffff0000, v26
	v_add_f32_e32 v26, v80, v16
	v_mul_f32_e32 v26, 0xbfb8aa3b, v26
	v_add_f32_e32 v80, v81, v17
	v_add_f32_e32 v78, 1.0, v78
	v_add_f32_e32 v79, 1.0, v79
	v_exp_f32_e32 v26, v26
	v_mul_f32_e32 v80, 0xbfb8aa3b, v80
	v_rcp_f32_e32 v78, v78
	v_rcp_f32_e32 v79, v79
	v_exp_f32_e32 v81, v80
	v_add_f32_e32 v74, v74, v10
	v_lshlrev_b32_e32 v94, 16, v106
	v_and_b32_e32 v95, 0xffff0000, v106
	v_add_f32_e32 v26, 1.0, v26
	v_mul_f32_e32 v74, 0xbfb8aa3b, v74
	v_pk_fma_f32 v[78:79], v[78:79], v[92:93], v[94:95]
	v_rcp_f32_e32 v80, v26
	v_add_f32_e32 v26, 1.0, v81
	v_exp_f32_e32 v94, v74
	v_add_f32_e32 v74, v75, v11
	v_rcp_f32_e32 v81, v26
	v_mul_f32_e32 v74, 0xbfb8aa3b, v74
	v_exp_f32_e32 v95, v74
	v_lshlrev_b32_e32 v26, 16, v27
	v_and_b32_e32 v27, 0xffff0000, v27
	v_lshlrev_b32_e32 v92, 16, v107
	v_and_b32_e32 v93, 0xffff0000, v107
	v_pk_fma_f32 v[74:75], v[80:81], v[26:27], v[92:93]
	v_lshlrev_b32_e32 v80, 16, v28
	v_and_b32_e32 v81, 0xffff0000, v28
	v_add_f32_e32 v28, v76, v12
	v_add_f32_e32 v76, v77, v13
	v_add_f32_e32 v26, 1.0, v94
	v_add_f32_e32 v27, 1.0, v95
	v_mul_f32_e32 v28, 0xbfb8aa3b, v28
	v_mul_f32_e32 v76, 0xbfb8aa3b, v76
	v_rcp_f32_e32 v26, v26
	v_rcp_f32_e32 v27, v27
	v_exp_f32_e32 v28, v28
	v_exp_f32_e32 v94, v76
	v_lshlrev_b32_e32 v92, 16, v104
	v_and_b32_e32 v93, 0xffff0000, v104
	v_pk_fma_f32 v[76:77], v[26:27], v[80:81], v[92:93]
	v_add_f32_e32 v26, 1.0, v28
	v_add_f32_e32 v27, 1.0, v94
	v_rcp_f32_e32 v26, v26
	v_rcp_f32_e32 v27, v27
	v_add_f32_e32 v70, v70, v6
	v_add_f32_e32 v71, v71, v7
	v_lshlrev_b32_e32 v28, 16, v29
	v_and_b32_e32 v29, 0xffff0000, v29
	v_lshlrev_b32_e32 v80, 16, v105
	v_and_b32_e32 v81, 0xffff0000, v105
	v_mul_f32_e32 v70, 0xbfb8aa3b, v70
	v_mul_f32_e32 v71, 0xbfb8aa3b, v71
	v_pk_fma_f32 v[80:81], v[26:27], v[28:29], v[80:81]
	v_exp_f32_e32 v70, v70
	v_exp_f32_e32 v71, v71
	v_cvt_pk_bf16_f32 v26, v78, v79
	v_cvt_pk_bf16_f32 v27, v74, v75
	v_cvt_pk_bf16_f32 v28, v76, v77
	v_cvt_pk_bf16_f32 v29, v80, v81
	v_lshl_add_u64 v[74:75], v[102:103], 0, v[0:1]
	ds_write_b128 v222, v[26:29] offset:16192
	s_mov_b64 exec, s[34:35]
	global_store_dwordx4 v[74:75], v[26:29], off
	s_mov_b64 exec, -1
	v_add_f32_e32 v66, v66, v2
	v_add_f32_e32 v67, v67, v3
	s_waitcnt vmcnt(5)
	v_lshlrev_b32_e32 v28, 16, v18
	v_and_b32_e32 v29, 0xffff0000, v18
	v_add_f32_e32 v18, v72, v8
	v_mul_f32_e32 v18, 0xbfb8aa3b, v18
	v_add_f32_e32 v72, v73, v9
	v_add_f32_e32 v26, 1.0, v70
	v_add_f32_e32 v27, 1.0, v71
	v_exp_f32_e32 v18, v18
	v_mul_f32_e32 v72, 0xbfb8aa3b, v72
	v_rcp_f32_e32 v26, v26
	v_rcp_f32_e32 v27, v27
	v_exp_f32_e32 v72, v72
	v_lshlrev_b32_e32 v70, 16, v100
	v_and_b32_e32 v71, 0xffff0000, v100
	v_add_f32_e32 v18, 1.0, v18
	v_pk_fma_f32 v[26:27], v[26:27], v[28:29], v[70:71]
	v_rcp_f32_e32 v28, v18
	v_add_f32_e32 v18, 1.0, v72
	v_mul_f32_e32 v66, 0xbfb8aa3b, v66
	v_mul_f32_e32 v67, 0xbfb8aa3b, v67
	v_rcp_f32_e32 v29, v18
	v_exp_f32_e32 v66, v66
	v_exp_f32_e32 v67, v67
	v_lshlrev_b32_e32 v18, 16, v19
	v_and_b32_e32 v19, 0xffff0000, v19
	v_lshlrev_b32_e32 v70, 16, v101
	v_and_b32_e32 v71, 0xffff0000, v101
	v_pk_fma_f32 v[28:29], v[28:29], v[18:19], v[70:71]
	v_add_f32_e32 v18, 1.0, v66
	v_add_f32_e32 v19, 1.0, v67
	v_lshlrev_b32_e32 v66, 16, v20
	v_and_b32_e32 v67, 0xffff0000, v20
	v_add_f32_e32 v20, v68, v4
	v_add_f32_e32 v68, v69, v5
	v_mul_f32_e32 v20, 0xbfb8aa3b, v20
	v_mul_f32_e32 v68, 0xbfb8aa3b, v68
	v_rcp_f32_e32 v18, v18
	v_rcp_f32_e32 v19, v19
	v_exp_f32_e32 v20, v20
	v_exp_f32_e32 v68, v68
	v_lshlrev_b32_e32 v70, 16, v98
	v_and_b32_e32 v71, 0xffff0000, v98
	v_pk_fma_f32 v[66:67], v[18:19], v[66:67], v[70:71]
	v_add_f32_e32 v18, 1.0, v20
	v_add_f32_e32 v19, 1.0, v68
	v_rcp_f32_e32 v18, v18
	v_rcp_f32_e32 v19, v19
	v_lshlrev_b32_e32 v20, 16, v21
	v_and_b32_e32 v21, 0xffff0000, v21
	v_lshlrev_b32_e32 v68, 16, v99
	v_and_b32_e32 v69, 0xffff0000, v99
	v_pk_fma_f32 v[68:69], v[18:19], v[20:21], v[68:69]
	v_cvt_pk_bf16_f32 v18, v26, v27
	v_cvt_pk_bf16_f32 v19, v28, v29
	v_cvt_pk_bf16_f32 v20, v66, v67
	v_cvt_pk_bf16_f32 v21, v68, v69
	ds_write_b128 v222, v[18:21] offset:24384
	s_mov_b64 exec, s[34:35]
	global_store_dwordx4 v[74:75], v[18:21], off offset:256
	s_mov_b64 exec, -1
	v_mov_b32_e32 v68, 0
	s_and_b64 vcc, exec, s[0:1]
	v_or_b32_e32 v20, 48, v114
	v_mov_b64_e32 v[18:19], s[12:13]
	v_mad_i64_i32 v[18:19], s[28:29], v20, s66, v[18:19]
	v_lshl_add_u64 v[18:19], s[26:27], 1, v[18:19]
	v_lshl_add_u64 v[18:19], v[18:19], 0, v[0:1]
	global_load_dwordx4 v[26:29], v[18:19], off
	v_ashrrev_i32_e32 v21, 31, v20
	v_lshlrev_b64 v[20:21], 11, v[20:21]
	v_lshl_add_u64 v[70:71], s[10:11], 0, v[20:21]
	v_mov_b32_e32 v74, 0
	v_mov_b32_e32 v75, 0
	v_mov_b32_e32 v72, 0
	v_mov_b32_e32 v73, 0
	s_cbranch_vccnz .LBB0_832
	v_lshl_add_u64 v[20:21], v[70:71], 0, v[0:1]
	global_load_dwordx2 v[74:75], v[20:21], off sc1
	global_load_dwordx2 v[72:73], v[20:21], off offset:8 sc1

	.amdhsa_kernel _Z4mega5KArgs
		.amdhsa_group_segment_fixed_size 16384
		.amdhsa_private_segment_fixed_size 0
		.amdhsa_kernarg_size 528
		.amdhsa_user_sgpr_count 2
		.amdhsa_user_sgpr_dispatch_ptr 0
		.amdhsa_user_sgpr_queue_ptr 0
		.amdhsa_user_sgpr_kernarg_segment_ptr 1
		.amdhsa_user_sgpr_dispatch_id 0
		.amdhsa_user_sgpr_kernarg_preload_length 0
		.amdhsa_user_sgpr_kernarg_preload_offset 0
		.amdhsa_user_sgpr_private_segment_size 0
		.amdhsa_uses_dynamic_stack 0
		.amdhsa_enable_private_segment 0
		.amdhsa_system_sgpr_workgroup_id_x 1
		.amdhsa_system_sgpr_workgroup_id_y 0
		.amdhsa_system_sgpr_workgroup_id_z 0
		.amdhsa_system_sgpr_workgroup_info 0
		.amdhsa_system_vgpr_workitem_id 0
		.amdhsa_next_free_vgpr 256
		.amdhsa_next_free_sgpr 100
		.amdhsa_accum_offset 256
		.amdhsa_reserve_vcc 1
		.amdhsa_float_round_mode_32 0
		.amdhsa_float_round_mode_16_64 0
		.amdhsa_float_denorm_mode_32 3
		.amdhsa_float_denorm_mode_16_64 3
		.amdhsa_dx10_clamp 1
		.amdhsa_ieee_mode 1
		.amdhsa_fp16_overflow 0
		.amdhsa_tg_split 0
		.amdhsa_exception_fp_ieee_invalid_op 0
		.amdhsa_exception_fp_denorm_src 0
		.amdhsa_exception_fp_ieee_div_zero 0
		.amdhsa_exception_fp_ieee_overflow 0
		.amdhsa_exception_fp_ieee_underflow 0
		.amdhsa_exception_fp_ieee_inexact 0
		.amdhsa_exception_int_div_zero 0
	.end_amdhsa_kernel

amdhsa.kernels:
  - .agpr_count:     0
    .args:
      - .offset:         0
        .size:           272
        .value_kind:     by_value
      - .offset:         272
        .size:           4
        .value_kind:     hidden_block_count_x
      - .offset:         276
        .size:           4
        .value_kind:     hidden_block_count_y
      - .offset:         280
        .size:           4
        .value_kind:     hidden_block_count_z
      - .offset:         284
        .size:           2
        .value_kind:     hidden_group_size_x
      - .offset:         286
        .size:           2
        .value_kind:     hidden_group_size_y
      - .offset:         288
        .size:           2
        .value_kind:     hidden_group_size_z
      - .offset:         290
        .size:           2
        .value_kind:     hidden_remainder_x
      - .offset:         292
        .size:           2
        .value_kind:     hidden_remainder_y
      - .offset:         294
        .size:           2
        .value_kind:     hidden_remainder_z
      - .offset:         312
        .size:           8
        .value_kind:     hidden_global_offset_x
      - .offset:         320
        .size:           8
        .value_kind:     hidden_global_offset_y
      - .offset:         328
        .size:           8
        .value_kind:     hidden_global_offset_z
      - .offset:         336
        .size:           2
        .value_kind:     hidden_grid_dims
      - .offset:         392
        .size:           4
        .value_kind:     hidden_dynamic_lds_size
    .group_segment_fixed_size: 16384
    .kernarg_segment_align: 8
    .kernarg_segment_size: 528
    .language:       OpenCL C
    .language_version:
      - 2
      - 0
    .max_flat_workgroup_size: 512
    .name:           _Z4mega5KArgs
    .private_segment_fixed_size: 0
    .sgpr_count:     106
    .sgpr_spill_count: 264
    .symbol:         _Z4mega5KArgs.kd
    .uniform_work_group_size: 1
    .uses_dynamic_stack: false
    .vgpr_count:     256
    .vgpr_spill_count: 0
    .wavefront_size: 64
